# moe2 GEMM epilogue (layer 0): residual rows prefetched in two batches of 8 loads instead of 16 serialized round trips
# speedup vs baseline: 1.0186x; 1.0014x over previous
.LBB0_2484:
	v_mov_b32_e32 v2, v180
	v_readlane_b32 s20, v254, 5
	v_and_b32_e32 v132, 15, v2
	v_lshl_add_u32 v139, v132, 2, s46
	ds_read_b32 v134, v139
	v_bfe_u32 v2, v2, 4, 2
	v_lshl_or_b32 v132, v2, 3, s47
	v_cmp_eq_u32_e64 s[0:1], 0, v2
	v_lshl_or_b32 v138, s49, 8, v132
	s_waitcnt lgkmcnt(0)
	v_max_i32_e32 v2, 0, v134
	v_lshlrev_b64 v[132:133], 10, v[2:3]
	v_readlane_b32 s21, v254, 6
	s_lshl_b32 s22, s49, 2
	v_or_b32_e32 v132, v132, v138
	v_cmp_lt_i32_e64 s[2:3], -1, v134
	s_mov_b64 s[4:5], -1
	s_and_b64 vcc, exec, s[20:21]
	s_cbranch_vccz .LBB0_2490
	s_load_dwordx2 s[100:101], s[8:9], 0x110
	ds_read_b32 v200, v139
	ds_read_b32 v202, v139 offset:64
	ds_read_b32 v204, v139 offset:128
	ds_read_b32 v206, v139 offset:192
	v_mov_b32_e32 v201, 0
	v_mov_b32_e32 v203, 0
	v_mov_b32_e32 v205, 0
	v_mov_b32_e32 v207, 0
	s_waitcnt lgkmcnt(0)
	v_max_i32_e32 v200, 0, v200
	v_max_i32_e32 v202, 0, v202
	v_max_i32_e32 v204, 0, v204
	v_max_i32_e32 v206, 0, v206
	v_lshlrev_b64 v[200:201], 10, v[200:201]
	v_lshlrev_b64 v[202:203], 10, v[202:203]
	v_lshlrev_b64 v[204:205], 10, v[204:205]
	v_lshlrev_b64 v[206:207], 10, v[206:207]
	v_or_b32_e32 v200, v200, v138
	v_or_b32_e32 v202, v202, v138
	v_or_b32_e32 v204, v204, v138
	v_or_b32_e32 v206, v206, v138
	v_lshl_add_u64 v[200:201], v[200:201], 1, s[100:101]
	v_lshl_add_u64 v[202:203], v[202:203], 1, s[100:101]
	v_lshl_add_u64 v[204:205], v[204:205], 1, s[100:101]
	v_lshl_add_u64 v[206:207], v[206:207], 1, s[100:101]
	global_load_dwordx4 v[160:163], v[200:201], off
	global_load_dwordx4 v[164:167], v[200:201], off offset:64
	global_load_dwordx4 v[168:171], v[202:203], off
	global_load_dwordx4 v[172:175], v[202:203], off offset:64
	global_load_dwordx4 v[176:179], v[204:205], off
	global_load_dwordx4 v[188:191], v[204:205], off offset:64
	global_load_dwordx4 v[192:195], v[206:207], off
	global_load_dwordx4 v[196:199], v[206:207], off offset:64
	s_waitcnt vmcnt(0)
	v_mov_b32_e32 v2, 0
	s_and_saveexec_b64 s[4:5], s[2:3]
	s_cbranch_execz .LBB0_2487
	s_load_dwordx2 s[20:21], s[8:9], 0x110
	s_waitcnt lgkmcnt(0)
	v_lshl_add_u64 v[144:145], v[132:133], 1, s[20:21]
	s_nop 1
	v_mov_b32_e32 v140, v160
	v_mov_b32_e32 v141, v161
	v_mov_b32_e32 v142, v162
	v_mov_b32_e32 v143, v163
	v_lshlrev_b32_e32 v136, 16, v140
	v_and_b32_e32 v137, 0xffff0000, v140
	v_lshlrev_b32_e32 v140, 16, v141
	v_and_b32_e32 v141, 0xffff0000, v141
	v_pk_add_f32 v[146:147], v[130:131], v[140:141]
	v_pk_add_f32 v[148:149], v[128:129], v[136:137]
	v_lshlrev_b32_e32 v140, 16, v142
	v_and_b32_e32 v141, 0xffff0000, v142
	v_lshlrev_b32_e32 v136, 16, v143
	v_and_b32_e32 v137, 0xffff0000, v143
	v_pk_add_f32 v[136:137], v[126:127], v[136:137]
	v_pk_add_f32 v[150:151], v[124:125], v[140:141]
	v_cvt_pk_bf16_f32 v140, v148, v149
	v_cvt_pk_bf16_f32 v141, v146, v147
	v_cvt_pk_bf16_f32 v142, v150, v151
	v_cvt_pk_bf16_f32 v143, v136, v137
	global_store_dwordx4 v[144:145], v[140:143], off
	s_nop 1
	v_mov_b32_e32 v140, v164
	v_mov_b32_e32 v141, v165
	v_mov_b32_e32 v142, v166
	v_mov_b32_e32 v143, v167
	v_lshlrev_b32_e32 v152, 16, v140
	v_and_b32_e32 v153, 0xffff0000, v140
	v_lshlrev_b32_e32 v140, 16, v141
	v_and_b32_e32 v141, 0xffff0000, v141
	v_pk_add_f32 v[154:155], v[122:123], v[140:141]
	v_lshlrev_b32_e32 v140, 16, v142
	v_and_b32_e32 v141, 0xffff0000, v142
	v_lshlrev_b32_e32 v142, 16, v143
	v_and_b32_e32 v143, 0xffff0000, v143
	v_pk_add_f32 v[152:153], v[120:121], v[152:153]
	v_pk_add_f32 v[156:157], v[118:119], v[142:143]
	v_pk_add_f32 v[158:159], v[116:117], v[140:141]
	v_cvt_pk_bf16_f32 v140, v152, v153
	v_cvt_pk_bf16_f32 v141, v154, v155
	v_cvt_pk_bf16_f32 v142, v158, v159
	v_cvt_pk_bf16_f32 v143, v156, v157
	global_store_dwordx4 v[144:145], v[140:143], off offset:64
	s_nop 1
	v_mov_b32_e32 v141, v152
	v_mov_b32_e32 v152, v149
	v_mov_b32_e32 v140, v148
	v_pk_mul_f32 v[142:143], v[152:153], v[152:153]
	s_nop 0
	v_pk_fma_f32 v[140:141], v[140:141], v[140:141], v[142:143]
	v_mov_b32_e32 v143, v154
	v_mov_b32_e32 v154, v147
	v_mov_b32_e32 v142, v146
	v_pk_mul_f32 v[144:145], v[154:155], v[154:155]
	s_nop 0
	v_pk_fma_f32 v[142:143], v[142:143], v[142:143], v[144:145]
	s_nop 0
	v_pk_add_f32 v[140:141], v[140:141], v[142:143]
	v_mov_b32_e32 v143, v158
	v_mov_b32_e32 v158, v151
	v_mov_b32_e32 v142, v150
	v_pk_mul_f32 v[144:145], v[158:159], v[158:159]
	s_nop 0
	v_pk_fma_f32 v[142:143], v[142:143], v[142:143], v[144:145]
	s_nop 0
	v_pk_add_f32 v[140:141], v[142:143], v[140:141]
	v_mov_b32_e32 v143, v156
	v_mov_b32_e32 v156, v137
	v_mov_b32_e32 v142, v136
	v_pk_mul_f32 v[136:137], v[156:157], v[156:157]
	s_nop 0
	v_pk_fma_f32 v[136:137], v[142:143], v[142:143], v[136:137]
	s_nop 0
	v_pk_add_f32 v[136:137], v[136:137], v[140:141]
	s_nop 0
	v_add_f32_e32 v2, v136, v137

.LBB0_2494:
	ds_read_b32 v118, v139 offset:64
	v_readlane_b32 s4, v254, 5
	v_readlane_b32 s5, v254, 6
	s_andn2_b64 vcc, exec, s[4:5]
	s_mov_b64 s[20:21], -1
	v_cndmask_b32_e64 v2, 0, 1, s[4:5]
	v_cmp_ne_u32_e64 s[2:3], 1, v2
	s_waitcnt lgkmcnt(0)
	v_max_i32_e32 v2, 0, v118
	v_lshlrev_b64 v[116:117], 10, v[2:3]
	v_cmp_lt_i32_e64 s[4:5], -1, v118
	v_or_b32_e32 v116, v116, v138
	s_cbranch_vccnz .LBB0_2500
	v_mov_b32_e32 v2, 0
	s_and_saveexec_b64 s[20:21], s[4:5]
	s_cbranch_execz .LBB0_2497
	s_load_dwordx2 s[24:25], s[8:9], 0x110
	s_waitcnt lgkmcnt(0)
	v_lshl_add_u64 v[126:127], v[116:117], 1, s[24:25]
	s_nop 1
	v_mov_b32_e32 v120, v168
	v_mov_b32_e32 v121, v169
	v_mov_b32_e32 v122, v170
	v_mov_b32_e32 v123, v171
	v_lshlrev_b32_e32 v124, 16, v120
	v_and_b32_e32 v125, 0xffff0000, v120
	v_lshlrev_b32_e32 v120, 16, v121
	v_and_b32_e32 v121, 0xffff0000, v121
	v_pk_add_f32 v[128:129], v[114:115], v[120:121]
	v_pk_add_f32 v[130:131], v[112:113], v[124:125]
	v_lshlrev_b32_e32 v124, 16, v122
	v_and_b32_e32 v125, 0xffff0000, v122
	v_lshlrev_b32_e32 v120, 16, v123
	v_and_b32_e32 v121, 0xffff0000, v123
	v_pk_add_f32 v[120:121], v[110:111], v[120:121]
	v_pk_add_f32 v[132:133], v[108:109], v[124:125]
	v_cvt_pk_bf16_f32 v122, v130, v131
	v_cvt_pk_bf16_f32 v123, v128, v129
	v_cvt_pk_bf16_f32 v124, v132, v133
	v_cvt_pk_bf16_f32 v125, v120, v121
	global_store_dwordx4 v[126:127], v[122:125], off
	s_nop 1
	v_mov_b32_e32 v122, v172
	v_mov_b32_e32 v123, v173
	v_mov_b32_e32 v124, v174
	v_mov_b32_e32 v125, v175
	v_lshlrev_b32_e32 v134, 16, v122
	v_and_b32_e32 v135, 0xffff0000, v122
	v_lshlrev_b32_e32 v122, 16, v123
	v_and_b32_e32 v123, 0xffff0000, v123
	v_pk_add_f32 v[136:137], v[106:107], v[122:123]
	v_lshlrev_b32_e32 v122, 16, v124
	v_and_b32_e32 v123, 0xffff0000, v124
	v_lshlrev_b32_e32 v124, 16, v125
	v_and_b32_e32 v125, 0xffff0000, v125
	v_pk_add_f32 v[134:135], v[104:105], v[134:135]
	v_pk_add_f32 v[140:141], v[102:103], v[124:125]
	v_pk_add_f32 v[142:143], v[100:101], v[122:123]
	v_cvt_pk_bf16_f32 v122, v134, v135
	v_cvt_pk_bf16_f32 v123, v136, v137
	v_cvt_pk_bf16_f32 v124, v142, v143
	v_cvt_pk_bf16_f32 v125, v140, v141
	global_store_dwordx4 v[126:127], v[122:125], off offset:64
	s_nop 1
	v_mov_b32_e32 v123, v134
	v_mov_b32_e32 v134, v131
	v_mov_b32_e32 v122, v130
	v_pk_mul_f32 v[124:125], v[134:135], v[134:135]
	s_nop 0
	v_pk_fma_f32 v[122:123], v[122:123], v[122:123], v[124:125]
	v_mov_b32_e32 v125, v136
	v_mov_b32_e32 v136, v129
	v_mov_b32_e32 v124, v128
	v_pk_mul_f32 v[126:127], v[136:137], v[136:137]
	s_nop 0
	v_pk_fma_f32 v[124:125], v[124:125], v[124:125], v[126:127]
	s_nop 0
	v_pk_add_f32 v[122:123], v[122:123], v[124:125]
	v_mov_b32_e32 v125, v142
	v_mov_b32_e32 v142, v133
	v_mov_b32_e32 v124, v132
	v_pk_mul_f32 v[126:127], v[142:143], v[142:143]
	s_nop 0
	v_pk_fma_f32 v[124:125], v[124:125], v[124:125], v[126:127]
	s_nop 0
	v_pk_add_f32 v[122:123], v[124:125], v[122:123]
	v_mov_b32_e32 v125, v140
	v_mov_b32_e32 v140, v121
	v_mov_b32_e32 v124, v120
	v_pk_mul_f32 v[120:121], v[140:141], v[140:141]
	s_nop 0
	v_pk_fma_f32 v[120:121], v[124:125], v[124:125], v[120:121]
	s_nop 0
	v_pk_add_f32 v[120:121], v[120:121], v[122:123]
	s_nop 0
	v_add_f32_e32 v2, v120, v121

.LBB0_2504:
	ds_read_b32 v102, v139 offset:128
	s_and_b64 vcc, exec, s[2:3]
	s_mov_b64 s[20:21], -1
	s_waitcnt lgkmcnt(0)
	v_max_i32_e32 v2, 0, v102
	v_lshlrev_b64 v[100:101], 10, v[2:3]
	v_cmp_lt_i32_e64 s[4:5], -1, v102
	v_or_b32_e32 v100, v100, v138
	s_cbranch_vccnz .LBB0_2510
	v_mov_b32_e32 v2, 0
	s_and_saveexec_b64 s[20:21], s[4:5]
	s_cbranch_execz .LBB0_2507
	s_load_dwordx2 s[24:25], s[8:9], 0x110
	s_waitcnt lgkmcnt(0)
	v_lshl_add_u64 v[110:111], v[100:101], 1, s[24:25]
	s_nop 1
	v_mov_b32_e32 v104, v176
	v_mov_b32_e32 v105, v177
	v_mov_b32_e32 v106, v178
	v_mov_b32_e32 v107, v179
	v_lshlrev_b32_e32 v108, 16, v104
	v_and_b32_e32 v109, 0xffff0000, v104
	v_lshlrev_b32_e32 v104, 16, v105
	v_and_b32_e32 v105, 0xffff0000, v105
	v_pk_add_f32 v[112:113], v[98:99], v[104:105]
	v_pk_add_f32 v[114:115], v[96:97], v[108:109]
	v_lshlrev_b32_e32 v108, 16, v106
	v_and_b32_e32 v109, 0xffff0000, v106
	v_lshlrev_b32_e32 v104, 16, v107
	v_and_b32_e32 v105, 0xffff0000, v107
	v_pk_add_f32 v[104:105], v[94:95], v[104:105]
	v_pk_add_f32 v[116:117], v[92:93], v[108:109]
	v_cvt_pk_bf16_f32 v106, v114, v115
	v_cvt_pk_bf16_f32 v107, v112, v113
	v_cvt_pk_bf16_f32 v108, v116, v117
	v_cvt_pk_bf16_f32 v109, v104, v105
	global_store_dwordx4 v[110:111], v[106:109], off
	s_nop 1
	v_mov_b32_e32 v106, v188
	v_mov_b32_e32 v107, v189
	v_mov_b32_e32 v108, v190
	v_mov_b32_e32 v109, v191
	v_lshlrev_b32_e32 v118, 16, v106
	v_and_b32_e32 v119, 0xffff0000, v106
	v_lshlrev_b32_e32 v106, 16, v107
	v_and_b32_e32 v107, 0xffff0000, v107
	v_pk_add_f32 v[120:121], v[90:91], v[106:107]
	v_lshlrev_b32_e32 v106, 16, v108
	v_and_b32_e32 v107, 0xffff0000, v108
	v_lshlrev_b32_e32 v108, 16, v109
	v_and_b32_e32 v109, 0xffff0000, v109
	v_pk_add_f32 v[118:119], v[88:89], v[118:119]
	v_pk_add_f32 v[122:123], v[86:87], v[108:109]
	v_pk_add_f32 v[124:125], v[84:85], v[106:107]
	v_cvt_pk_bf16_f32 v106, v118, v119
	v_cvt_pk_bf16_f32 v107, v120, v121
	v_cvt_pk_bf16_f32 v108, v124, v125
	v_cvt_pk_bf16_f32 v109, v122, v123
	global_store_dwordx4 v[110:111], v[106:109], off offset:64
	s_nop 1
	v_mov_b32_e32 v107, v118
	v_mov_b32_e32 v118, v115
	v_mov_b32_e32 v106, v114
	v_pk_mul_f32 v[108:109], v[118:119], v[118:119]
	s_nop 0
	v_pk_fma_f32 v[106:107], v[106:107], v[106:107], v[108:109]
	v_mov_b32_e32 v109, v120
	v_mov_b32_e32 v120, v113
	v_mov_b32_e32 v108, v112
	v_pk_mul_f32 v[110:111], v[120:121], v[120:121]
	s_nop 0
	v_pk_fma_f32 v[108:109], v[108:109], v[108:109], v[110:111]
	s_nop 0
	v_pk_add_f32 v[106:107], v[106:107], v[108:109]
	v_mov_b32_e32 v109, v124
	v_mov_b32_e32 v124, v117
	v_mov_b32_e32 v108, v116
	v_pk_mul_f32 v[110:111], v[124:125], v[124:125]
	s_nop 0
	v_pk_fma_f32 v[108:109], v[108:109], v[108:109], v[110:111]
	s_nop 0
	v_pk_add_f32 v[106:107], v[108:109], v[106:107]
	v_mov_b32_e32 v109, v122
	v_mov_b32_e32 v122, v105
	v_mov_b32_e32 v108, v104
	v_pk_mul_f32 v[104:105], v[122:123], v[122:123]
	s_nop 0
	v_pk_fma_f32 v[104:105], v[108:109], v[108:109], v[104:105]
	s_nop 0
	v_pk_add_f32 v[104:105], v[104:105], v[106:107]
	s_nop 0
	v_add_f32_e32 v2, v104, v105

.LBB0_2514:
	ds_read_b32 v86, v139 offset:192
	s_and_b64 vcc, exec, s[2:3]
	s_mov_b64 s[20:21], -1
	s_waitcnt lgkmcnt(0)
	v_max_i32_e32 v2, 0, v86
	v_lshlrev_b64 v[84:85], 10, v[2:3]
	v_cmp_lt_i32_e64 s[4:5], -1, v86
	v_or_b32_e32 v84, v84, v138
	s_cbranch_vccnz .LBB0_2520
	v_mov_b32_e32 v2, 0
	s_and_saveexec_b64 s[20:21], s[4:5]
	s_cbranch_execz .LBB0_2517
	s_load_dwordx2 s[24:25], s[8:9], 0x110
	s_waitcnt lgkmcnt(0)
	v_lshl_add_u64 v[94:95], v[84:85], 1, s[24:25]
	s_nop 1
	v_mov_b32_e32 v88, v192
	v_mov_b32_e32 v89, v193
	v_mov_b32_e32 v90, v194
	v_mov_b32_e32 v91, v195
	v_lshlrev_b32_e32 v92, 16, v88
	v_and_b32_e32 v93, 0xffff0000, v88
	v_lshlrev_b32_e32 v88, 16, v89
	v_and_b32_e32 v89, 0xffff0000, v89
	v_pk_add_f32 v[96:97], v[82:83], v[88:89]
	v_pk_add_f32 v[98:99], v[80:81], v[92:93]
	v_lshlrev_b32_e32 v92, 16, v90
	v_and_b32_e32 v93, 0xffff0000, v90
	v_lshlrev_b32_e32 v88, 16, v91
	v_and_b32_e32 v89, 0xffff0000, v91
	v_pk_add_f32 v[88:89], v[78:79], v[88:89]
	v_pk_add_f32 v[100:101], v[76:77], v[92:93]
	v_cvt_pk_bf16_f32 v90, v98, v99
	v_cvt_pk_bf16_f32 v91, v96, v97
	v_cvt_pk_bf16_f32 v92, v100, v101
	v_cvt_pk_bf16_f32 v93, v88, v89
	global_store_dwordx4 v[94:95], v[90:93], off
	s_nop 1
	v_mov_b32_e32 v90, v196
	v_mov_b32_e32 v91, v197
	v_mov_b32_e32 v92, v198
	v_mov_b32_e32 v93, v199
	v_lshlrev_b32_e32 v102, 16, v90
	v_and_b32_e32 v103, 0xffff0000, v90
	v_lshlrev_b32_e32 v90, 16, v91
	v_and_b32_e32 v91, 0xffff0000, v91
	v_pk_add_f32 v[104:105], v[74:75], v[90:91]
	v_lshlrev_b32_e32 v90, 16, v92
	v_and_b32_e32 v91, 0xffff0000, v92
	v_lshlrev_b32_e32 v92, 16, v93
	v_and_b32_e32 v93, 0xffff0000, v93
	v_pk_add_f32 v[102:103], v[72:73], v[102:103]
	v_pk_add_f32 v[106:107], v[70:71], v[92:93]
	v_pk_add_f32 v[108:109], v[68:69], v[90:91]
	v_cvt_pk_bf16_f32 v90, v102, v103
	v_cvt_pk_bf16_f32 v91, v104, v105
	v_cvt_pk_bf16_f32 v92, v108, v109
	v_cvt_pk_bf16_f32 v93, v106, v107
	global_store_dwordx4 v[94:95], v[90:93], off offset:64
	s_nop 1
	v_mov_b32_e32 v91, v102
	v_mov_b32_e32 v102, v99
	v_mov_b32_e32 v90, v98
	v_pk_mul_f32 v[92:93], v[102:103], v[102:103]
	s_nop 0
	v_pk_fma_f32 v[90:91], v[90:91], v[90:91], v[92:93]
	v_mov_b32_e32 v93, v104
	v_mov_b32_e32 v104, v97
	v_mov_b32_e32 v92, v96
	v_pk_mul_f32 v[94:95], v[104:105], v[104:105]
	s_nop 0
	v_pk_fma_f32 v[92:93], v[92:93], v[92:93], v[94:95]
	s_nop 0
	v_pk_add_f32 v[90:91], v[90:91], v[92:93]
	v_mov_b32_e32 v93, v108
	v_mov_b32_e32 v108, v101
	v_mov_b32_e32 v92, v100
	v_pk_mul_f32 v[94:95], v[108:109], v[108:109]
	s_nop 0
	v_pk_fma_f32 v[92:93], v[92:93], v[92:93], v[94:95]
	s_nop 0
	v_pk_add_f32 v[90:91], v[92:93], v[90:91]
	v_mov_b32_e32 v93, v106
	v_mov_b32_e32 v106, v89
	v_mov_b32_e32 v92, v88
	v_pk_mul_f32 v[88:89], v[106:107], v[106:107]
	s_nop 0
	v_pk_fma_f32 v[88:89], v[92:93], v[92:93], v[88:89]
	s_nop 0
	v_pk_add_f32 v[88:89], v[88:89], v[90:91]
	s_nop 0
	v_add_f32_e32 v2, v88, v89

.LBB0_2524:
	ds_read_b32 v70, v139 offset:256
	s_and_b64 vcc, exec, s[2:3]
	s_mov_b64 s[20:21], -1
	s_waitcnt lgkmcnt(0)
	v_max_i32_e32 v2, 0, v70
	v_lshlrev_b64 v[68:69], 10, v[2:3]
	v_cmp_lt_i32_e64 s[4:5], -1, v70
	v_or_b32_e32 v68, v68, v138
	s_cbranch_vccnz .LBB0_2530
	s_load_dwordx2 s[100:101], s[8:9], 0x110
	ds_read_b32 v200, v139 offset:256
	ds_read_b32 v202, v139 offset:320
	ds_read_b32 v204, v139 offset:384
	ds_read_b32 v206, v139 offset:448
	v_mov_b32_e32 v201, 0
	v_mov_b32_e32 v203, 0
	v_mov_b32_e32 v205, 0
	v_mov_b32_e32 v207, 0
	s_waitcnt lgkmcnt(0)
	v_max_i32_e32 v200, 0, v200
	v_max_i32_e32 v202, 0, v202
	v_max_i32_e32 v204, 0, v204
	v_max_i32_e32 v206, 0, v206
	v_lshlrev_b64 v[200:201], 10, v[200:201]
	v_lshlrev_b64 v[202:203], 10, v[202:203]
	v_lshlrev_b64 v[204:205], 10, v[204:205]
	v_lshlrev_b64 v[206:207], 10, v[206:207]
	v_or_b32_e32 v200, v200, v138
	v_or_b32_e32 v202, v202, v138
	v_or_b32_e32 v204, v204, v138
	v_or_b32_e32 v206, v206, v138
	v_lshl_add_u64 v[200:201], v[200:201], 1, s[100:101]
	v_lshl_add_u64 v[202:203], v[202:203], 1, s[100:101]
	v_lshl_add_u64 v[204:205], v[204:205], 1, s[100:101]
	v_lshl_add_u64 v[206:207], v[206:207], 1, s[100:101]
	global_load_dwordx4 v[160:163], v[200:201], off
	global_load_dwordx4 v[164:167], v[200:201], off offset:64
	global_load_dwordx4 v[168:171], v[202:203], off
	global_load_dwordx4 v[172:175], v[202:203], off offset:64
	global_load_dwordx4 v[176:179], v[204:205], off
	global_load_dwordx4 v[188:191], v[204:205], off offset:64
	global_load_dwordx4 v[192:195], v[206:207], off
	global_load_dwordx4 v[196:199], v[206:207], off offset:64
	s_waitcnt vmcnt(0)
	v_mov_b32_e32 v2, 0
	s_and_saveexec_b64 s[20:21], s[4:5]
	s_cbranch_execz .LBB0_2527
	s_load_dwordx2 s[24:25], s[8:9], 0x110
	s_waitcnt lgkmcnt(0)
	v_lshl_add_u64 v[78:79], v[68:69], 1, s[24:25]
	s_nop 1
	v_mov_b32_e32 v72, v160
	v_mov_b32_e32 v73, v161
	v_mov_b32_e32 v74, v162
	v_mov_b32_e32 v75, v163
	v_lshlrev_b32_e32 v76, 16, v72
	v_and_b32_e32 v77, 0xffff0000, v72
	v_lshlrev_b32_e32 v72, 16, v73
	v_and_b32_e32 v73, 0xffff0000, v73
	v_pk_add_f32 v[80:81], v[66:67], v[72:73]
	v_pk_add_f32 v[82:83], v[64:65], v[76:77]
	v_lshlrev_b32_e32 v76, 16, v74
	v_and_b32_e32 v77, 0xffff0000, v74
	v_lshlrev_b32_e32 v72, 16, v75
	v_and_b32_e32 v73, 0xffff0000, v75
	v_pk_add_f32 v[72:73], v[62:63], v[72:73]
	v_pk_add_f32 v[84:85], v[60:61], v[76:77]
	v_cvt_pk_bf16_f32 v74, v82, v83
	v_cvt_pk_bf16_f32 v75, v80, v81
	v_cvt_pk_bf16_f32 v76, v84, v85
	v_cvt_pk_bf16_f32 v77, v72, v73
	global_store_dwordx4 v[78:79], v[74:77], off
	s_nop 1
	v_mov_b32_e32 v74, v164
	v_mov_b32_e32 v75, v165
	v_mov_b32_e32 v76, v166
	v_mov_b32_e32 v77, v167
	v_lshlrev_b32_e32 v86, 16, v74
	v_and_b32_e32 v87, 0xffff0000, v74
	v_lshlrev_b32_e32 v74, 16, v75
	v_and_b32_e32 v75, 0xffff0000, v75
	v_pk_add_f32 v[88:89], v[58:59], v[74:75]
	v_lshlrev_b32_e32 v74, 16, v76
	v_and_b32_e32 v75, 0xffff0000, v76
	v_lshlrev_b32_e32 v76, 16, v77
	v_and_b32_e32 v77, 0xffff0000, v77
	v_pk_add_f32 v[86:87], v[56:57], v[86:87]
	v_pk_add_f32 v[90:91], v[54:55], v[76:77]
	v_pk_add_f32 v[92:93], v[52:53], v[74:75]
	v_cvt_pk_bf16_f32 v74, v86, v87
	v_cvt_pk_bf16_f32 v75, v88, v89
	v_cvt_pk_bf16_f32 v76, v92, v93
	v_cvt_pk_bf16_f32 v77, v90, v91
	global_store_dwordx4 v[78:79], v[74:77], off offset:64
	s_nop 1
	v_mov_b32_e32 v75, v86
	v_mov_b32_e32 v86, v83
	v_mov_b32_e32 v74, v82
	v_pk_mul_f32 v[76:77], v[86:87], v[86:87]
	s_nop 0
	v_pk_fma_f32 v[74:75], v[74:75], v[74:75], v[76:77]
	v_mov_b32_e32 v77, v88
	v_mov_b32_e32 v88, v81
	v_mov_b32_e32 v76, v80
	v_pk_mul_f32 v[78:79], v[88:89], v[88:89]
	s_nop 0
	v_pk_fma_f32 v[76:77], v[76:77], v[76:77], v[78:79]
	s_nop 0
	v_pk_add_f32 v[74:75], v[74:75], v[76:77]
	v_mov_b32_e32 v77, v92
	v_mov_b32_e32 v92, v85
	v_mov_b32_e32 v76, v84
	v_pk_mul_f32 v[78:79], v[92:93], v[92:93]
	s_nop 0
	v_pk_fma_f32 v[76:77], v[76:77], v[76:77], v[78:79]
	s_nop 0
	v_pk_add_f32 v[74:75], v[76:77], v[74:75]
	v_mov_b32_e32 v77, v90
	v_mov_b32_e32 v90, v73
	v_mov_b32_e32 v76, v72
	v_pk_mul_f32 v[72:73], v[90:91], v[90:91]
	s_nop 0
	v_pk_fma_f32 v[72:73], v[76:77], v[76:77], v[72:73]
	s_nop 0
	v_pk_add_f32 v[72:73], v[72:73], v[74:75]
	s_nop 0
	v_add_f32_e32 v2, v72, v73

.LBB0_2534:
	ds_read_b32 v54, v139 offset:320
	s_and_b64 vcc, exec, s[2:3]
	s_mov_b64 s[20:21], -1
	s_waitcnt lgkmcnt(0)
	v_max_i32_e32 v2, 0, v54
	v_lshlrev_b64 v[52:53], 10, v[2:3]
	v_cmp_lt_i32_e64 s[4:5], -1, v54
	v_or_b32_e32 v52, v52, v138
	s_cbranch_vccnz .LBB0_2540
	v_mov_b32_e32 v2, 0
	s_and_saveexec_b64 s[20:21], s[4:5]
	s_cbranch_execz .LBB0_2537
	s_load_dwordx2 s[24:25], s[8:9], 0x110
	s_waitcnt lgkmcnt(0)
	v_lshl_add_u64 v[62:63], v[52:53], 1, s[24:25]
	s_nop 1
	v_mov_b32_e32 v56, v168
	v_mov_b32_e32 v57, v169
	v_mov_b32_e32 v58, v170
	v_mov_b32_e32 v59, v171
	v_lshlrev_b32_e32 v60, 16, v56
	v_and_b32_e32 v61, 0xffff0000, v56
	v_lshlrev_b32_e32 v56, 16, v57
	v_and_b32_e32 v57, 0xffff0000, v57
	v_pk_add_f32 v[64:65], v[50:51], v[56:57]
	v_pk_add_f32 v[66:67], v[48:49], v[60:61]
	v_lshlrev_b32_e32 v60, 16, v58
	v_and_b32_e32 v61, 0xffff0000, v58
	v_lshlrev_b32_e32 v56, 16, v59
	v_and_b32_e32 v57, 0xffff0000, v59
	v_pk_add_f32 v[56:57], v[46:47], v[56:57]
	v_pk_add_f32 v[68:69], v[44:45], v[60:61]
	v_cvt_pk_bf16_f32 v58, v66, v67
	v_cvt_pk_bf16_f32 v59, v64, v65
	v_cvt_pk_bf16_f32 v60, v68, v69
	v_cvt_pk_bf16_f32 v61, v56, v57
	global_store_dwordx4 v[62:63], v[58:61], off
	s_nop 1
	v_mov_b32_e32 v58, v172
	v_mov_b32_e32 v59, v173
	v_mov_b32_e32 v60, v174
	v_mov_b32_e32 v61, v175
	v_lshlrev_b32_e32 v70, 16, v58
	v_and_b32_e32 v71, 0xffff0000, v58
	v_lshlrev_b32_e32 v58, 16, v59
	v_and_b32_e32 v59, 0xffff0000, v59
	v_pk_add_f32 v[72:73], v[42:43], v[58:59]
	v_lshlrev_b32_e32 v58, 16, v60
	v_and_b32_e32 v59, 0xffff0000, v60
	v_lshlrev_b32_e32 v60, 16, v61
	v_and_b32_e32 v61, 0xffff0000, v61
	v_pk_add_f32 v[70:71], v[40:41], v[70:71]
	v_pk_add_f32 v[74:75], v[38:39], v[60:61]
	v_pk_add_f32 v[76:77], v[36:37], v[58:59]
	v_cvt_pk_bf16_f32 v58, v70, v71
	v_cvt_pk_bf16_f32 v59, v72, v73
	v_cvt_pk_bf16_f32 v60, v76, v77
	v_cvt_pk_bf16_f32 v61, v74, v75
	global_store_dwordx4 v[62:63], v[58:61], off offset:64
	s_nop 1
	v_mov_b32_e32 v59, v70
	v_mov_b32_e32 v70, v67
	v_mov_b32_e32 v58, v66
	v_pk_mul_f32 v[60:61], v[70:71], v[70:71]
	s_nop 0
	v_pk_fma_f32 v[58:59], v[58:59], v[58:59], v[60:61]
	v_mov_b32_e32 v61, v72
	v_mov_b32_e32 v72, v65
	v_mov_b32_e32 v60, v64
	v_pk_mul_f32 v[62:63], v[72:73], v[72:73]
	s_nop 0
	v_pk_fma_f32 v[60:61], v[60:61], v[60:61], v[62:63]
	s_nop 0
	v_pk_add_f32 v[58:59], v[58:59], v[60:61]
	v_mov_b32_e32 v61, v76
	v_mov_b32_e32 v76, v69
	v_mov_b32_e32 v60, v68
	v_pk_mul_f32 v[62:63], v[76:77], v[76:77]
	s_nop 0
	v_pk_fma_f32 v[60:61], v[60:61], v[60:61], v[62:63]
	s_nop 0
	v_pk_add_f32 v[58:59], v[60:61], v[58:59]
	v_mov_b32_e32 v61, v74
	v_mov_b32_e32 v74, v57
	v_mov_b32_e32 v60, v56
	v_pk_mul_f32 v[56:57], v[74:75], v[74:75]
	s_nop 0
	v_pk_fma_f32 v[56:57], v[60:61], v[60:61], v[56:57]
	s_nop 0
	v_pk_add_f32 v[56:57], v[56:57], v[58:59]
	s_nop 0
	v_add_f32_e32 v2, v56, v57

.LBB0_2544:
	ds_read_b32 v38, v139 offset:384
	s_and_b64 vcc, exec, s[2:3]
	s_mov_b64 s[20:21], -1
	s_waitcnt lgkmcnt(0)
	v_max_i32_e32 v2, 0, v38
	v_lshlrev_b64 v[36:37], 10, v[2:3]
	v_cmp_lt_i32_e64 s[4:5], -1, v38
	v_or_b32_e32 v36, v36, v138
	s_cbranch_vccnz .LBB0_2550
	v_mov_b32_e32 v2, 0
	s_and_saveexec_b64 s[20:21], s[4:5]
	s_cbranch_execz .LBB0_2547
	s_load_dwordx2 s[24:25], s[8:9], 0x110
	s_waitcnt lgkmcnt(0)
	v_lshl_add_u64 v[46:47], v[36:37], 1, s[24:25]
	s_nop 1
	v_mov_b32_e32 v40, v176
	v_mov_b32_e32 v41, v177
	v_mov_b32_e32 v42, v178
	v_mov_b32_e32 v43, v179
	v_lshlrev_b32_e32 v44, 16, v40
	v_and_b32_e32 v45, 0xffff0000, v40
	v_lshlrev_b32_e32 v40, 16, v41
	v_and_b32_e32 v41, 0xffff0000, v41
	v_pk_add_f32 v[48:49], v[34:35], v[40:41]
	v_pk_add_f32 v[50:51], v[32:33], v[44:45]
	v_lshlrev_b32_e32 v44, 16, v42
	v_and_b32_e32 v45, 0xffff0000, v42
	v_lshlrev_b32_e32 v40, 16, v43
	v_and_b32_e32 v41, 0xffff0000, v43
	v_pk_add_f32 v[40:41], v[30:31], v[40:41]
	v_pk_add_f32 v[52:53], v[28:29], v[44:45]
	v_cvt_pk_bf16_f32 v42, v50, v51
	v_cvt_pk_bf16_f32 v43, v48, v49
	v_cvt_pk_bf16_f32 v44, v52, v53
	v_cvt_pk_bf16_f32 v45, v40, v41
	global_store_dwordx4 v[46:47], v[42:45], off
	s_nop 1
	v_mov_b32_e32 v42, v188
	v_mov_b32_e32 v43, v189
	v_mov_b32_e32 v44, v190
	v_mov_b32_e32 v45, v191
	v_lshlrev_b32_e32 v54, 16, v42
	v_and_b32_e32 v55, 0xffff0000, v42
	v_lshlrev_b32_e32 v42, 16, v43
	v_and_b32_e32 v43, 0xffff0000, v43
	v_pk_add_f32 v[56:57], v[26:27], v[42:43]
	v_lshlrev_b32_e32 v42, 16, v44
	v_and_b32_e32 v43, 0xffff0000, v44
	v_lshlrev_b32_e32 v44, 16, v45
	v_and_b32_e32 v45, 0xffff0000, v45
	v_pk_add_f32 v[54:55], v[24:25], v[54:55]
	v_pk_add_f32 v[58:59], v[22:23], v[44:45]
	v_pk_add_f32 v[60:61], v[20:21], v[42:43]
	v_cvt_pk_bf16_f32 v42, v54, v55
	v_cvt_pk_bf16_f32 v43, v56, v57
	v_cvt_pk_bf16_f32 v44, v60, v61
	v_cvt_pk_bf16_f32 v45, v58, v59
	global_store_dwordx4 v[46:47], v[42:45], off offset:64
	s_nop 1
	v_mov_b32_e32 v43, v54
	v_mov_b32_e32 v54, v51
	v_mov_b32_e32 v42, v50
	v_pk_mul_f32 v[44:45], v[54:55], v[54:55]
	s_nop 0
	v_pk_fma_f32 v[42:43], v[42:43], v[42:43], v[44:45]
	v_mov_b32_e32 v45, v56
	v_mov_b32_e32 v56, v49
	v_mov_b32_e32 v44, v48
	v_pk_mul_f32 v[46:47], v[56:57], v[56:57]
	s_nop 0
	v_pk_fma_f32 v[44:45], v[44:45], v[44:45], v[46:47]
	s_nop 0
	v_pk_add_f32 v[42:43], v[42:43], v[44:45]
	v_mov_b32_e32 v45, v60
	v_mov_b32_e32 v60, v53
	v_mov_b32_e32 v44, v52
	v_pk_mul_f32 v[46:47], v[60:61], v[60:61]
	s_nop 0
	v_pk_fma_f32 v[44:45], v[44:45], v[44:45], v[46:47]
	s_nop 0
	v_pk_add_f32 v[42:43], v[44:45], v[42:43]
	v_mov_b32_e32 v45, v58
	v_mov_b32_e32 v58, v41
	v_mov_b32_e32 v44, v40
	v_pk_mul_f32 v[40:41], v[58:59], v[58:59]
	s_nop 0
	v_pk_fma_f32 v[40:41], v[44:45], v[44:45], v[40:41]
	s_nop 0
	v_pk_add_f32 v[40:41], v[40:41], v[42:43]
	s_nop 0
	v_add_f32_e32 v2, v40, v41

.LBB0_2554:
	ds_read_b32 v22, v139 offset:448
	s_and_b64 vcc, exec, s[2:3]
	s_mov_b64 s[4:5], -1
	s_waitcnt lgkmcnt(0)
	v_max_i32_e32 v2, 0, v22
	v_lshlrev_b64 v[20:21], 10, v[2:3]
	v_cmp_lt_i32_e64 s[2:3], -1, v22
	v_or_b32_e32 v20, v20, v138
	s_cbranch_vccnz .LBB0_2560
	v_mov_b32_e32 v2, 0
	s_and_saveexec_b64 s[4:5], s[2:3]
	s_cbranch_execz .LBB0_2557
	s_load_dwordx2 s[20:21], s[8:9], 0x110
	s_waitcnt lgkmcnt(0)
	v_lshl_add_u64 v[30:31], v[20:21], 1, s[20:21]
	s_nop 1
	v_mov_b32_e32 v24, v192
	v_mov_b32_e32 v25, v193
	v_mov_b32_e32 v26, v194
	v_mov_b32_e32 v27, v195
	v_lshlrev_b32_e32 v28, 16, v24
	v_and_b32_e32 v29, 0xffff0000, v24
	v_lshlrev_b32_e32 v24, 16, v25
	v_and_b32_e32 v25, 0xffff0000, v25
	v_pk_add_f32 v[32:33], v[18:19], v[24:25]
	v_pk_add_f32 v[34:35], v[16:17], v[28:29]
	v_lshlrev_b32_e32 v28, 16, v26
	v_and_b32_e32 v29, 0xffff0000, v26
	v_lshlrev_b32_e32 v24, 16, v27
	v_and_b32_e32 v25, 0xffff0000, v27
	v_pk_add_f32 v[24:25], v[14:15], v[24:25]
	v_pk_add_f32 v[36:37], v[12:13], v[28:29]
	v_cvt_pk_bf16_f32 v26, v34, v35
	v_cvt_pk_bf16_f32 v27, v32, v33
	v_cvt_pk_bf16_f32 v28, v36, v37
	v_cvt_pk_bf16_f32 v29, v24, v25
	global_store_dwordx4 v[30:31], v[26:29], off
	s_nop 1
	v_mov_b32_e32 v26, v196
	v_mov_b32_e32 v27, v197
	v_mov_b32_e32 v28, v198
	v_mov_b32_e32 v29, v199
	v_lshlrev_b32_e32 v38, 16, v26
	v_and_b32_e32 v39, 0xffff0000, v26
	v_lshlrev_b32_e32 v26, 16, v27
	v_and_b32_e32 v27, 0xffff0000, v27
	v_pk_add_f32 v[40:41], v[10:11], v[26:27]
	v_lshlrev_b32_e32 v26, 16, v28
	v_and_b32_e32 v27, 0xffff0000, v28
	v_lshlrev_b32_e32 v28, 16, v29
	v_and_b32_e32 v29, 0xffff0000, v29
	v_pk_add_f32 v[38:39], v[8:9], v[38:39]
	v_pk_add_f32 v[42:43], v[6:7], v[28:29]
	v_pk_add_f32 v[44:45], v[4:5], v[26:27]
	v_cvt_pk_bf16_f32 v26, v38, v39
	v_cvt_pk_bf16_f32 v27, v40, v41
	v_cvt_pk_bf16_f32 v28, v44, v45
	v_cvt_pk_bf16_f32 v29, v42, v43
	global_store_dwordx4 v[30:31], v[26:29], off offset:64
	s_nop 1
	v_mov_b32_e32 v27, v38
	v_mov_b32_e32 v38, v35
	v_mov_b32_e32 v26, v34
	v_pk_mul_f32 v[28:29], v[38:39], v[38:39]
	s_nop 0
	v_pk_fma_f32 v[26:27], v[26:27], v[26:27], v[28:29]
	v_mov_b32_e32 v29, v40
	v_mov_b32_e32 v40, v33
	v_mov_b32_e32 v28, v32
	v_pk_mul_f32 v[30:31], v[40:41], v[40:41]
	s_nop 0
	v_pk_fma_f32 v[28:29], v[28:29], v[28:29], v[30:31]
	s_nop 0
	v_pk_add_f32 v[26:27], v[26:27], v[28:29]
	v_mov_b32_e32 v29, v44
	v_mov_b32_e32 v44, v37
	v_mov_b32_e32 v28, v36
	v_pk_mul_f32 v[30:31], v[44:45], v[44:45]
	s_nop 0
	v_pk_fma_f32 v[28:29], v[28:29], v[28:29], v[30:31]
	s_nop 0
	v_pk_add_f32 v[26:27], v[28:29], v[26:27]
	v_mov_b32_e32 v29, v42
	v_mov_b32_e32 v42, v25
	v_mov_b32_e32 v28, v24
	v_pk_mul_f32 v[24:25], v[42:43], v[42:43]
	s_nop 0
	v_pk_fma_f32 v[24:25], v[28:29], v[28:29], v[24:25]
	s_nop 0
	v_pk_add_f32 v[24:25], v[24:25], v[26:27]
	s_nop 0
	v_add_f32_e32 v2, v24, v25
